# phase F: top-4 selection and LayerNorm wave sums rewritten with DPP/permlane instead of ds_bpermute ladders (bit-identical results)
# speedup vs baseline: 1.0044x; 1.0044x over previous
.LBB0_873:
	v_lshlrev_b32_e32 v151, 16, v129
	v_lshlrev_b32_e32 v150, 16, v128
	v_and_b32_e32 v149, 0xffff0000, v129
	v_and_b32_e32 v148, 0xffff0000, v128
	v_lshlrev_b32_e32 v147, 16, v127
	v_lshlrev_b32_e32 v146, 16, v126
	v_and_b32_e32 v145, 0xffff0000, v127
	v_and_b32_e32 v144, 0xffff0000, v126
	v_pk_add_f32 v[128:129], v[150:151], v[148:149]
	v_pk_add_f32 v[154:155], v[146:147], v[144:145]
	v_add_f32_e32 v128, v128, v129
	v_lshlrev_b32_e32 v138, 16, v124
	v_and_b32_e32 v139, 0xffff0000, v124
	v_lshlrev_b32_e32 v140, 16, v125
	v_and_b32_e32 v141, 0xffff0000, v125
	v_lshlrev_b32_e32 v143, 16, v152
	v_and_b32_e32 v129, 0xffff0000, v152
	v_lshlrev_b32_e32 v127, 16, v153
	v_and_b32_e32 v125, 0xffff0000, v153
	v_pk_add_f32 v[152:153], v[154:155], v[154:155] op_sel:[0,1] op_sel_hi:[1,0]
	v_add_f32_e32 v142, 0, v128
	v_add_f32_e32 v126, v138, v139
	v_add_f32_e32 v124, v140, v141
	v_mov_b32_e32 v153, v129
	v_pk_add_f32 v[152:153], v[142:143], v[152:153]
	v_pk_add_f32 v[154:155], v[126:127], v[124:125]
	s_add_i32 s61, s60, s59
	v_pk_add_f32 v[152:153], v[152:153], v[154:155]
	s_nop 0
	v_add_f32_e32 v124, v152, v153
	v_mov_b32_e32 v205, v124
	s_nop 1
	v_add_f32_dpp v205, v205, v205 quad_perm:[1,0,3,2] row_mask:0xf bank_mask:0xf
	s_nop 1
	v_add_f32_dpp v205, v205, v205 quad_perm:[2,3,0,1] row_mask:0xf bank_mask:0xf
	s_nop 1
	v_add_f32_dpp v205, v205, v205 row_half_mirror row_mask:0xf bank_mask:0xf
	s_nop 1
	v_add_f32_dpp v205, v205, v205 row_mirror row_mask:0xf bank_mask:0xf
	s_nop 1
	v_add_f32_dpp v205, v205, v205 row_bcast:15 row_mask:0xa bank_mask:0xf
	s_nop 1
	v_add_f32_dpp v205, v205, v205 row_bcast:31 row_mask:0xc bank_mask:0xf
	s_nop 1
	v_readlane_b32 s82, v205, 63
	s_waitcnt lgkmcnt(0)
	s_waitcnt lgkmcnt(0)
	s_waitcnt lgkmcnt(0)
	s_waitcnt lgkmcnt(0)
	s_waitcnt lgkmcnt(0)
	s_waitcnt lgkmcnt(0)
	s_nop 1
	v_mov_b32_e32 v124, s82
	v_fmac_f32_e32 v149, 0xba800000, v124
	v_fmac_f32_e32 v148, 0xba800000, v124
	v_fmac_f32_e32 v151, 0xba800000, v124
	v_fmac_f32_e32 v150, 0xba800000, v124
	v_mul_f32_e32 v126, v148, v148
	v_mul_f32_e32 v128, v149, v149
	v_fmac_f32_e32 v126, v150, v150
	v_fmac_f32_e32 v128, v151, v151
	v_fmac_f32_e32 v145, 0xba800000, v124
	v_fmac_f32_e32 v144, 0xba800000, v124
	v_add_f32_e32 v126, v126, v128
	v_fmac_f32_e32 v147, 0xba800000, v124
	v_fmac_f32_e32 v146, 0xba800000, v124
	v_mul_f32_e32 v128, v144, v144
	v_mul_f32_e32 v142, v145, v145
	v_fmac_f32_e32 v128, v146, v146
	v_fmac_f32_e32 v142, v147, v147
	v_add_f32_e32 v128, v128, v142
	v_fmac_f32_e32 v141, 0xba800000, v124
	v_fmac_f32_e32 v139, 0xba800000, v124
	v_add_f32_e32 v126, v126, v128
	v_fmac_f32_e32 v140, 0xba800000, v124
	v_fmac_f32_e32 v138, 0xba800000, v124
	v_mul_f32_e32 v128, v139, v139
	v_mul_f32_e32 v142, v141, v141
	v_fmac_f32_e32 v128, v138, v138
	v_fmac_f32_e32 v142, v140, v140
	v_add_f32_e32 v128, v128, v142
	v_fmac_f32_e32 v125, 0xba800000, v124
	v_fmac_f32_e32 v129, 0xba800000, v124
	v_add_f32_e32 v126, v128, v126
	v_fmac_f32_e32 v127, 0xba800000, v124
	v_fmac_f32_e32 v143, 0xba800000, v124
	v_mul_f32_e32 v128, v129, v129
	v_mul_f32_e32 v142, v125, v125
	v_fmac_f32_e32 v128, v143, v143
	v_fmac_f32_e32 v142, v127, v127
	v_add_f32_e32 v128, v128, v142
	v_add_f32_e32 v126, v128, v126
	v_mov_b32_e32 v206, v126
	s_nop 1
	v_add_f32_dpp v206, v206, v206 quad_perm:[1,0,3,2] row_mask:0xf bank_mask:0xf
	s_nop 1
	v_add_f32_dpp v206, v206, v206 quad_perm:[2,3,0,1] row_mask:0xf bank_mask:0xf
	s_nop 1
	v_add_f32_dpp v206, v206, v206 row_half_mirror row_mask:0xf bank_mask:0xf
	s_nop 1
	v_add_f32_dpp v206, v206, v206 row_mirror row_mask:0xf bank_mask:0xf
	s_nop 1
	v_add_f32_dpp v206, v206, v206 row_bcast:15 row_mask:0xa bank_mask:0xf
	s_nop 1
	v_add_f32_dpp v206, v206, v206 row_bcast:31 row_mask:0xc bank_mask:0xf
	s_nop 1
	v_readlane_b32 s83, v206, 63
	s_waitcnt lgkmcnt(0)
	s_waitcnt lgkmcnt(0)
	s_waitcnt lgkmcnt(0)
	s_waitcnt lgkmcnt(0)
	s_waitcnt lgkmcnt(0)
	s_waitcnt lgkmcnt(0)
	s_nop 1
	v_mov_b32_e32 v126, s83
	v_fmamk_f32 v126, v126, 0x3a800000, v240
	v_mul_f32_e32 v128, 0x4f800000, v126
	v_cmp_gt_f32_e32 vcc, s36, v126
	s_nop 1
	v_cndmask_b32_e32 v126, v126, v128, vcc
	v_sqrt_f32_e32 v128, v126
	s_nop 0
	v_add_u32_e32 v142, -1, v128
	v_fma_f32 v152, -v142, v128, v126
	v_cmp_ge_f32_e64 s[16:17], 0, v152
	v_add_u32_e32 v152, 1, v128
	s_nop 0
	v_cndmask_b32_e64 v142, v128, v142, s[16:17]
	v_fma_f32 v128, -v152, v128, v126
	v_cmp_lt_f32_e64 s[16:17], 0, v128
	s_nop 1
	v_cndmask_b32_e64 v128, v142, v152, s[16:17]
	v_mul_f32_e32 v142, 0x37800000, v128
	v_cndmask_b32_e32 v128, v128, v142, vcc
	v_cmp_class_f32_e32 vcc, v126, v234
	s_nop 1
	v_cndmask_b32_e32 v126, v128, v126, vcc
	v_div_scale_f32 v128, s[16:17], v126, v126, 1.0
	v_rcp_f32_e32 v142, v128
	s_add_i32 s16, s61, s54
	s_ashr_i32 s17, s16, 31
	v_fma_f32 v152, -v128, v142, 1.0
	v_fmac_f32_e32 v142, v152, v142
	v_div_scale_f32 v152, vcc, 1.0, v126, 1.0
	v_mul_f32_e32 v153, v152, v142
	v_fma_f32 v154, -v128, v153, v152
	v_fmac_f32_e32 v153, v154, v142
	v_fma_f32 v128, -v128, v153, v152
	v_div_fmas_f32 v128, v128, v142, v153
	v_div_fixup_f32 v126, v128, v126, 1.0
	s_and_saveexec_b64 s[26:27], s[6:7]
	s_cbranch_execz .LBB0_875
	s_lshl_b64 s[62:63], s[16:17], 3
	s_add_u32 s62, s39, s62
	v_mul_f32_e32 v152, 0x3a800000, v124
	s_addc_u32 s63, s45, s63
	v_mov_b32_e32 v153, v126
	global_store_dwordx2 v215, v[152:153], s[62:63]
.LBB0_875:
	s_or_b64 exec, exec, s[26:27]
	v_mov_b32_e32 v152, v150
	v_mov_b32_e32 v153, v148
	v_mov_b32_e32 v148, v151
	v_pk_mul_f32 v[150:151], v[152:153], v[126:127] op_sel_hi:[1,0]
	v_mov_b32_e32 v155, v144
	v_pk_fma_f32 v[150:151], v[2:3], v[150:151], v[10:11]
	v_pk_mul_f32 v[148:149], v[148:149], v[126:127] op_sel_hi:[1,0]
	v_cvt_pk_bf16_f32 v144, v151, 0
	v_cvt_pk_bf16_f32 v124, v150, 0
	v_lshlrev_b32_e32 v153, 16, v144
	v_lshlrev_b32_e32 v152, 16, v124
	v_and_or_b32 v180, v124, s37, v153
	v_mov_b32_e32 v124, v215
	v_cvt_pk_fp8_f32 v124, v150, v151
	v_pk_fma_f32 v[148:149], v[4:5], v[148:149], v[12:13]
	v_mov_b32_e32 v154, v146
	v_cvt_pk_bf16_f32 v146, v148, 0
	v_cvt_pk_bf16_f32 v156, v149, 0
	v_cvt_pk_fp8_f32 v124, v148, v149 op_sel:[0,0,1]
	v_mov_b32_e32 v144, v147
	v_pk_add_f32 v[152:153], v[150:151], v[152:153] neg_lo:[0,1] neg_hi:[0,1]
	v_lshlrev_b32_e32 v150, 16, v146
	v_lshlrev_b32_e32 v151, 16, v156
	v_pk_mul_f32 v[144:145], v[144:145], v[126:127] op_sel_hi:[1,0]
	s_lshl_b64 s[16:17], s[16:17], 10
	v_and_or_b32 v181, v146, s37, v151
	v_pk_add_f32 v[148:149], v[148:149], v[150:151] neg_lo:[0,1] neg_hi:[0,1]
	v_pk_mul_f32 v[146:147], v[154:155], v[126:127] op_sel_hi:[1,0]
	v_pk_fma_f32 v[184:185], v[8:9], v[144:145], v[16:17]
	v_mov_b32_e32 v128, v143
	v_lshl_add_u64 v[142:143], v[104:105], 0, s[16:17]
	v_cvt_pk_bf16_f32 v183, v148, v149
	v_pk_fma_f32 v[144:145], v[6:7], v[146:147], v[14:15]
	v_cvt_pk_bf16_f32 v149, v185, 0
	global_store_dword v[142:143], v124, off
	v_cvt_pk_bf16_f32 v124, v144, 0
	v_cvt_pk_bf16_f32 v146, v145, 0
	v_cvt_pk_bf16_f32 v148, v184, 0
	v_lshlrev_b32_e32 v191, 16, v149
	v_cvt_pk_bf16_f32 v182, v152, v153
	v_lshlrev_b32_e32 v147, 16, v146
	v_lshlrev_b32_e32 v146, 16, v124
	v_lshlrev_b32_e32 v190, 16, v148
	v_and_or_b32 v187, v148, s37, v191
	v_lshlrev_b32_e32 v155, 16, v137
	v_lshlrev_b32_e32 v154, 16, v136
	v_and_b32_e32 v153, 0xffff0000, v137
	v_and_b32_e32 v152, 0xffff0000, v136
	v_lshlrev_b32_e32 v151, 16, v135
	v_lshlrev_b32_e32 v150, 16, v134
	v_and_b32_e32 v149, 0xffff0000, v135
	v_and_b32_e32 v148, 0xffff0000, v134
	v_and_or_b32 v186, v124, s37, v147
	v_pk_add_f32 v[146:147], v[144:145], v[146:147] neg_lo:[0,1] neg_hi:[0,1]
	v_mov_b32_e32 v124, v215
	v_pk_add_f32 v[136:137], v[154:155], v[152:153]
	v_pk_add_f32 v[192:193], v[150:151], v[148:149]
	v_cvt_pk_bf16_f32 v188, v146, v147
	v_cvt_pk_fp8_f32 v124, v144, v145
	v_add_f32_e32 v136, v136, v137
	v_lshlrev_b32_e32 v144, 16, v132
	v_and_b32_e32 v145, 0xffff0000, v132
	v_lshlrev_b32_e32 v146, 16, v133
	v_and_b32_e32 v147, 0xffff0000, v133
	v_lshlrev_b32_e32 v157, 16, v130
	v_and_b32_e32 v137, 0xffff0000, v130
	v_lshlrev_b32_e32 v135, 16, v131
	v_and_b32_e32 v133, 0xffff0000, v131
	v_pk_add_f32 v[130:131], v[192:193], v[192:193] op_sel:[0,1] op_sel_hi:[1,0]
	v_add_f32_e32 v156, 0, v136
	v_add_f32_e32 v134, v144, v145
	v_add_f32_e32 v132, v146, v147
	v_mov_b32_e32 v131, v137
	v_pk_add_f32 v[130:131], v[156:157], v[130:131]
	v_pk_add_f32 v[192:193], v[134:135], v[132:133]
	v_cvt_pk_fp8_f32 v124, v184, v185 op_sel:[0,0,1]
	v_pk_add_f32 v[130:131], v[130:131], v[192:193]
	v_pk_mul_f32 v[138:139], v[138:139], v[126:127] op_sel_hi:[1,0]
	v_add_f32_e32 v132, v130, v131
	v_mov_b32_e32 v207, v132
	s_nop 1
	v_add_f32_dpp v207, v207, v207 quad_perm:[1,0,3,2] row_mask:0xf bank_mask:0xf
	s_nop 1
	v_add_f32_dpp v207, v207, v207 quad_perm:[2,3,0,1] row_mask:0xf bank_mask:0xf
	s_nop 1
	v_add_f32_dpp v207, v207, v207 row_half_mirror row_mask:0xf bank_mask:0xf
	s_nop 1
	v_add_f32_dpp v207, v207, v207 row_mirror row_mask:0xf bank_mask:0xf
	s_nop 1
	v_add_f32_dpp v207, v207, v207 row_bcast:15 row_mask:0xa bank_mask:0xf
	s_nop 1
	v_add_f32_dpp v207, v207, v207 row_bcast:31 row_mask:0xc bank_mask:0xf
	s_nop 1
	v_readlane_b32 s84, v207, 63
	global_store_dword v[142:143], v124, off offset:256
	v_pk_add_f32 v[130:131], v[184:185], v[190:191] neg_lo:[0,1] neg_hi:[0,1]
	ds_write2st64_b64 v176, v[180:181], v[186:187] offset1:1
	v_cvt_pk_bf16_f32 v189, v130, v131
	s_waitcnt lgkmcnt(1)
	v_pk_mul_f32 v[130:131], v[140:141], v[126:127] op_sel_hi:[1,0]
	v_add_u32_e32 v134, 0x100, v176
	v_pk_fma_f32 v[140:141], v[20:21], v[130:131], v[28:29]
	v_pk_fma_f32 v[130:131], v[18:19], v[138:139], v[26:27]
	s_waitcnt lgkmcnt(0)
	v_cvt_pk_bf16_f32 v138, v131, 0
	v_cvt_pk_bf16_f32 v136, v130, 0
	v_lshlrev_b32_e32 v139, 16, v138
	v_lshlrev_b32_e32 v138, 16, v136
	s_waitcnt lgkmcnt(0)
	v_and_or_b32 v180, v136, s37, v139
	v_mov_b32_e32 v136, v215
	v_pk_add_f32 v[138:139], v[130:131], v[138:139] neg_lo:[0,1] neg_hi:[0,1]
	v_cvt_pk_fp8_f32 v136, v130, v131
	s_waitcnt lgkmcnt(0)
	v_cvt_pk_bf16_f32 v156, v140, 0
	v_cvt_pk_bf16_f32 v179, v141, 0
	ds_write2st64_b64 v134, v[182:183], v[188:189] offset0:64 offset1:65
	v_lshlrev_b32_e32 v182, 16, v156
	s_waitcnt lgkmcnt(1)
	v_lshlrev_b32_e32 v183, 16, v179
	v_cvt_pk_fp8_f32 v136, v140, v141 op_sel:[0,0,1]
	v_pk_add_f32 v[140:141], v[140:141], v[182:183] neg_lo:[0,1] neg_hi:[0,1]
	v_cvt_pk_bf16_f32 v138, v138, v139
	s_waitcnt lgkmcnt(0)
	s_nop 1
	v_mov_b32_e32 v130, s84
	v_fmac_f32_e32 v153, 0xba800000, v130
	v_fmac_f32_e32 v152, 0xba800000, v130
	v_fmac_f32_e32 v155, 0xba800000, v130
	v_fmac_f32_e32 v154, 0xba800000, v130
	v_mul_f32_e32 v124, v152, v152
	v_mul_f32_e32 v131, v153, v153
	v_fmac_f32_e32 v124, v154, v154
	v_fmac_f32_e32 v131, v155, v155
	v_fmac_f32_e32 v149, 0xba800000, v130
	v_fmac_f32_e32 v148, 0xba800000, v130
	v_add_f32_e32 v124, v124, v131
	v_fmac_f32_e32 v151, 0xba800000, v130
	v_fmac_f32_e32 v150, 0xba800000, v130
	v_mul_f32_e32 v131, v148, v148
	v_mul_f32_e32 v132, v149, v149
	v_fmac_f32_e32 v131, v150, v150
	v_fmac_f32_e32 v132, v151, v151
	v_add_f32_e32 v131, v131, v132
	v_fmac_f32_e32 v147, 0xba800000, v130
	v_fmac_f32_e32 v145, 0xba800000, v130
	v_add_f32_e32 v124, v124, v131
	v_fmac_f32_e32 v146, 0xba800000, v130
	v_fmac_f32_e32 v144, 0xba800000, v130
	v_mul_f32_e32 v131, v145, v145
	v_mul_f32_e32 v132, v147, v147
	v_fmac_f32_e32 v131, v144, v144
	v_fmac_f32_e32 v132, v146, v146
	v_add_f32_e32 v131, v131, v132
	v_fmac_f32_e32 v133, 0xba800000, v130
	v_fmac_f32_e32 v137, 0xba800000, v130
	v_add_f32_e32 v124, v131, v124
	v_fmac_f32_e32 v135, 0xba800000, v130
	v_fmac_f32_e32 v157, 0xba800000, v130
	v_mul_f32_e32 v131, v137, v137
	v_mul_f32_e32 v132, v133, v133
	v_fmac_f32_e32 v131, v157, v157
	v_fmac_f32_e32 v132, v135, v135
	v_add_f32_e32 v131, v131, v132
	v_add_f32_e32 v124, v131, v124
	v_mov_b32_e32 v208, v124
	s_nop 1
	v_add_f32_dpp v208, v208, v208 quad_perm:[1,0,3,2] row_mask:0xf bank_mask:0xf
	s_nop 1
	v_add_f32_dpp v208, v208, v208 quad_perm:[2,3,0,1] row_mask:0xf bank_mask:0xf
	s_nop 1
	v_add_f32_dpp v208, v208, v208 row_half_mirror row_mask:0xf bank_mask:0xf
	s_nop 1
	v_add_f32_dpp v208, v208, v208 row_mirror row_mask:0xf bank_mask:0xf
	s_nop 1
	v_add_f32_dpp v208, v208, v208 row_bcast:15 row_mask:0xa bank_mask:0xf
	s_nop 1
	v_add_f32_dpp v208, v208, v208 row_bcast:31 row_mask:0xc bank_mask:0xf
	s_nop 1
	v_readlane_b32 s85, v208, 63
	v_cvt_pk_bf16_f32 v139, v140, v141
	v_and_or_b32 v181, v156, s37, v183
	global_store_dword v[142:143], v136, off offset:512
	s_waitcnt lgkmcnt(0)
	v_mov_b32_e32 v124, v127
	v_pk_mul_f32 v[124:125], v[124:125], v[126:127] op_sel_hi:[1,0]
	v_pk_mul_f32 v[126:127], v[128:129], v[126:127] op_sel_hi:[1,0]
	v_pk_fma_f32 v[124:125], v[24:25], v[124:125], v[32:33]
	s_waitcnt lgkmcnt(0)
	v_pk_fma_f32 v[126:127], v[22:23], v[126:127], v[30:31]
	v_cvt_pk_bf16_f32 v136, v124, 0
	v_cvt_pk_bf16_f32 v132, v127, 0
	v_cvt_pk_bf16_f32 v131, v126, 0
	s_waitcnt lgkmcnt(0)
	v_lshlrev_b32_e32 v129, 16, v132
	v_lshlrev_b32_e32 v128, 16, v131
	v_and_or_b32 v140, v131, s37, v129
	v_pk_add_f32 v[128:129], v[126:127], v[128:129] neg_lo:[0,1] neg_hi:[0,1]
	s_waitcnt lgkmcnt(0)
	v_cvt_pk_bf16_f32 v128, v128, v129
	v_mov_b32_e32 v156, v215
	v_cvt_pk_fp8_f32 v156, v126, v127
	v_cvt_pk_bf16_f32 v179, v125, 0
	s_waitcnt lgkmcnt(0)
	v_lshlrev_b32_e32 v126, 16, v136
	v_lshlrev_b32_e32 v127, 16, v179
	v_cvt_pk_fp8_f32 v156, v124, v125 op_sel:[0,0,1]
	v_pk_add_f32 v[124:125], v[124:125], v[126:127] neg_lo:[0,1] neg_hi:[0,1]
	s_waitcnt lgkmcnt(0)
	s_nop 1
	v_mov_b32_e32 v129, s85
	v_fmamk_f32 v129, v129, 0x3a800000, v240
	v_mul_f32_e32 v131, 0x4f800000, v129
	v_cmp_gt_f32_e32 vcc, s36, v129
	v_and_or_b32 v141, v136, s37, v127
	global_store_dword v[142:143], v156, off offset:768
	v_cndmask_b32_e32 v131, v129, v131, vcc
	v_sqrt_f32_e32 v132, v131
	v_cvt_pk_bf16_f32 v129, v124, v125
	ds_write2st64_b64 v176, v[180:181], v[140:141] offset0:2 offset1:3
	ds_write2st64_b64 v134, v[138:139], v[128:129] offset0:66 offset1:67
	v_add_u32_e32 v124, -1, v132
	v_fma_f32 v125, -v124, v132, v131
	v_cmp_ge_f32_e64 s[16:17], 0, v125
	v_add_u32_e32 v125, 1, v132
	v_fma_f32 v126, -v125, v132, v131
	v_cndmask_b32_e64 v124, v132, v124, s[16:17]
	v_cmp_lt_f32_e64 s[16:17], 0, v126
	s_nop 1
	v_cndmask_b32_e64 v124, v124, v125, s[16:17]
	v_mul_f32_e32 v125, 0x37800000, v124
	v_cndmask_b32_e32 v124, v124, v125, vcc
	v_cmp_class_f32_e32 vcc, v131, v234
	s_nop 1
	v_cndmask_b32_e32 v124, v124, v131, vcc
	v_div_scale_f32 v125, s[16:17], v124, v124, 1.0
	v_rcp_f32_e32 v126, v125
	s_add_i32 s16, s61, s56
	s_ashr_i32 s17, s16, 31
	v_fma_f32 v127, -v125, v126, 1.0
	v_fmac_f32_e32 v126, v127, v126
	v_div_scale_f32 v127, vcc, 1.0, v124, 1.0
	v_mul_f32_e32 v128, v127, v126
	v_fma_f32 v129, -v125, v128, v127
	v_fmac_f32_e32 v128, v129, v126
	v_fma_f32 v125, -v125, v128, v127
	v_div_fmas_f32 v125, v125, v126, v128
	v_div_fixup_f32 v124, v125, v124, 1.0
	s_and_saveexec_b64 s[26:27], s[6:7]
	s_cbranch_execz .LBB0_877
	s_lshl_b64 s[62:63], s[16:17], 3
	s_add_u32 s62, s39, s62
	v_mul_f32_e32 v126, 0x3a800000, v130
	s_addc_u32 s63, s45, s63
	v_mov_b32_e32 v127, v124
	global_store_dwordx2 v215, v[126:127], s[62:63]
.LBB0_877:
	s_or_b64 exec, exec, s[26:27]
	v_mov_b32_e32 v126, v154
	v_mov_b32_e32 v127, v152
	v_pk_mul_f32 v[126:127], v[126:127], v[124:125] op_sel_hi:[1,0]
	v_mov_b32_e32 v152, v155
	v_pk_fma_f32 v[126:127], v[2:3], v[126:127], v[10:11]
	v_pk_mul_f32 v[138:139], v[152:153], v[124:125] op_sel_hi:[1,0]
	v_cvt_pk_bf16_f32 v132, v127, 0
	v_cvt_pk_bf16_f32 v125, v126, 0
	v_lshlrev_b32_e32 v141, 16, v132
	v_lshlrev_b32_e32 v140, 16, v125
	v_and_or_b32 v142, v125, s37, v141
	v_mov_b32_e32 v125, v215
	v_cvt_pk_fp8_f32 v125, v126, v127
	v_pk_fma_f32 v[138:139], v[4:5], v[138:139], v[12:13]
	v_mov_b32_e32 v128, v150
	v_mov_b32_e32 v129, v148
	v_cvt_pk_fp8_f32 v125, v138, v139 op_sel:[0,0,1]
	v_cvt_pk_bf16_f32 v134, v138, 0
	v_cvt_pk_bf16_f32 v143, v139, 0
	v_pk_add_f32 v[140:141], v[126:127], v[140:141] neg_lo:[0,1] neg_hi:[0,1]
	v_pk_mul_f32 v[128:129], v[128:129], v[124:125] op_sel_hi:[1,0]
	s_lshl_b64 s[16:17], s[16:17], 10
	v_cvt_pk_bf16_f32 v126, v140, v141
	v_lshlrev_b32_e32 v140, 16, v134
	v_lshlrev_b32_e32 v141, 16, v143
	v_pk_fma_f32 v[128:129], v[6:7], v[128:129], v[14:15]
	v_lshl_add_u64 v[130:131], v[104:105], 0, s[16:17]
	v_pk_add_f32 v[138:139], v[138:139], v[140:141] neg_lo:[0,1] neg_hi:[0,1]
	v_mov_b32_e32 v148, v151
	v_cvt_pk_bf16_f32 v132, v129, 0
	v_and_or_b32 v143, v134, s37, v141
	v_cvt_pk_bf16_f32 v127, v138, v139
	global_store_dword v[130:131], v125, off
	v_pk_mul_f32 v[138:139], v[148:149], v[124:125] op_sel_hi:[1,0]
	v_cvt_pk_bf16_f32 v125, v128, 0
	v_lshlrev_b32_e32 v141, 16, v132
	v_lshlrev_b32_e32 v140, 16, v125
	v_and_or_b32 v148, v125, s37, v141
	v_mov_b32_e32 v125, v215
	v_cvt_pk_fp8_f32 v125, v128, v129
	v_pk_fma_f32 v[138:139], v[8:9], v[138:139], v[16:17]
	v_pk_add_f32 v[140:141], v[128:129], v[140:141] neg_lo:[0,1] neg_hi:[0,1]
	v_cvt_pk_bf16_f32 v134, v138, 0
	v_cvt_pk_bf16_f32 v149, v139, 0
	v_cvt_pk_fp8_f32 v125, v138, v139 op_sel:[0,0,1]
	v_cvt_pk_bf16_f32 v128, v140, v141
	v_lshlrev_b32_e32 v140, 16, v134
	v_lshlrev_b32_e32 v141, 16, v149
	v_and_or_b32 v149, v134, s37, v141
	v_pk_add_f32 v[138:139], v[138:139], v[140:141] neg_lo:[0,1] neg_hi:[0,1]
	ds_write2st64_b64 v177, v[142:143], v[148:149] offset1:1
	v_cvt_pk_bf16_f32 v129, v138, v139
	v_add_u32_e32 v142, 0x100, v177
	ds_write2st64_b64 v142, v[126:127], v[128:129] offset0:64 offset1:65
	v_pk_mul_f32 v[128:129], v[144:145], v[124:125] op_sel_hi:[1,0]
	global_store_dword v[130:131], v125, off offset:256
	v_pk_fma_f32 v[128:129], v[18:19], v[128:129], v[26:27]
	v_pk_mul_f32 v[126:127], v[146:147], v[124:125] op_sel_hi:[1,0]
	v_cvt_pk_bf16_f32 v132, v129, 0
	v_cvt_pk_bf16_f32 v125, v128, 0
	v_lshlrev_b32_e32 v139, 16, v132
	v_lshlrev_b32_e32 v138, 16, v125
	v_and_or_b32 v140, v125, s37, v139
	v_mov_b32_e32 v125, v215
	v_cvt_pk_fp8_f32 v125, v128, v129
	v_pk_fma_f32 v[126:127], v[20:21], v[126:127], v[28:29]
	v_pk_add_f32 v[138:139], v[128:129], v[138:139] neg_lo:[0,1] neg_hi:[0,1]
	v_cvt_pk_bf16_f32 v134, v126, 0
	v_cvt_pk_fp8_f32 v125, v126, v127 op_sel:[0,0,1]
	v_cvt_pk_bf16_f32 v141, v127, 0
	v_cvt_pk_bf16_f32 v128, v138, v139
	v_lshlrev_b32_e32 v138, 16, v134
	v_lshlrev_b32_e32 v139, 16, v141
	v_mov_b32_e32 v136, v157
	v_pk_add_f32 v[126:127], v[126:127], v[138:139] neg_lo:[0,1] neg_hi:[0,1]
	v_mov_b32_e32 v132, v135
	v_cvt_pk_bf16_f32 v129, v126, v127
	global_store_dword v[130:131], v125, off offset:512
	v_pk_mul_f32 v[126:127], v[132:133], v[124:125] op_sel_hi:[1,0]
	v_pk_mul_f32 v[124:125], v[136:137], v[124:125] op_sel_hi:[1,0]
	v_mov_b32_e32 v137, v215
	v_pk_fma_f32 v[124:125], v[22:23], v[124:125], v[30:31]
	v_and_or_b32 v141, v134, s37, v139
	v_cvt_pk_fp8_f32 v137, v124, v125
	v_cvt_pk_bf16_f32 v134, v124, 0
	v_cvt_pk_bf16_f32 v132, v125, 0
	v_pk_fma_f32 v[126:127], v[24:25], v[126:127], v[32:33]
	v_lshlrev_b32_e32 v133, 16, v132
	v_lshlrev_b32_e32 v132, 16, v134
	v_cvt_pk_bf16_f32 v135, v126, 0
	v_cvt_pk_bf16_f32 v136, v127, 0
	v_and_or_b32 v134, v134, s37, v133
	v_pk_add_f32 v[132:133], v[124:125], v[132:133] neg_lo:[0,1] neg_hi:[0,1]
	v_cvt_pk_fp8_f32 v137, v126, v127 op_sel:[0,0,1]
	v_cvt_pk_bf16_f32 v124, v132, v133
	v_lshlrev_b32_e32 v132, 16, v135
	v_lshlrev_b32_e32 v133, 16, v136
	v_pk_add_f32 v[126:127], v[126:127], v[132:133] neg_lo:[0,1] neg_hi:[0,1]
	v_and_or_b32 v135, v135, s37, v133
	v_cvt_pk_bf16_f32 v125, v126, v127
	global_store_dword v[130:131], v137, off offset:768
	ds_write2st64_b64 v177, v[140:141], v[134:135] offset0:2 offset1:3
	ds_write2st64_b64 v142, v[128:129], v[124:125] offset0:66 offset1:67
	s_waitcnt lgkmcnt(0)
	s_barrier
	ds_read_b128 v[124:127], v167
	ds_read_b128 v[132:135], v167 offset:33024
	s_waitcnt lgkmcnt(1)
	v_mfma_f32_16x16x32_bf16 v[128:131], v[124:127], v[34:37], 0
	v_mfma_f32_16x16x32_bf16 v[136:139], v[124:127], v[70:73], 0
	s_waitcnt lgkmcnt(0)
	v_mfma_f32_16x16x32_bf16 v[128:131], v[132:135], v[34:37], v[128:131]
	v_mfma_f32_16x16x32_bf16 v[132:135], v[132:135], v[70:73], v[136:139]
	v_mfma_f32_16x16x32_bf16 v[128:131], v[124:127], v[38:41], v[128:131]
	s_nop 3
	ds_read_b128 v[136:139], v167 offset:33088
	v_mfma_f32_16x16x32_bf16 v[124:127], v[124:127], v[74:77], v[132:135]
	s_nop 2
	ds_read_b128 v[132:135], v167 offset:64
	s_waitcnt lgkmcnt(0)
	v_mfma_f32_16x16x32_bf16 v[128:131], v[132:135], v[42:45], v[128:131]
	v_mfma_f32_16x16x32_bf16 v[124:127], v[132:135], v[78:81], v[124:127]
	v_mfma_f32_16x16x32_bf16 v[128:131], v[136:139], v[42:45], v[128:131]
	v_mfma_f32_16x16x32_bf16 v[124:127], v[136:139], v[78:81], v[124:127]
	ds_read_b128 v[136:139], v167 offset:33152
	v_mfma_f32_16x16x32_bf16 v[128:131], v[132:135], v[46:49], v[128:131]
	v_mfma_f32_16x16x32_bf16 v[124:127], v[132:135], v[82:85], v[124:127]
	ds_read_b128 v[132:135], v167 offset:128
	s_waitcnt lgkmcnt(0)
	v_mfma_f32_16x16x32_bf16 v[128:131], v[132:135], v[50:53], v[128:131]
	v_mfma_f32_16x16x32_bf16 v[124:127], v[132:135], v[86:89], v[124:127]
	v_mfma_f32_16x16x32_bf16 v[128:131], v[136:139], v[50:53], v[128:131]
	v_mfma_f32_16x16x32_bf16 v[124:127], v[136:139], v[86:89], v[124:127]
	ds_read_b128 v[136:139], v167 offset:33216
	v_mfma_f32_16x16x32_bf16 v[128:131], v[132:135], v[54:57], v[128:131]
	v_mfma_f32_16x16x32_bf16 v[124:127], v[132:135], v[90:93], v[124:127]
	ds_read_b128 v[132:135], v167 offset:192
	s_waitcnt lgkmcnt(0)
	v_mfma_f32_16x16x32_bf16 v[128:131], v[132:135], v[58:61], v[128:131]
	v_mfma_f32_16x16x32_bf16 v[124:127], v[132:135], v[94:97], v[124:127]
	v_mfma_f32_16x16x32_bf16 v[128:131], v[136:139], v[58:61], v[128:131]
	v_mfma_f32_16x16x32_bf16 v[124:127], v[136:139], v[94:97], v[124:127]
	v_mfma_f32_16x16x32_bf16 v[128:131], v[132:135], v[62:65], v[128:131]
	v_mfma_f32_16x16x32_bf16 v[124:127], v[132:135], v[98:101], v[124:127]
	s_nop 7
	ds_write2_b32 v178, v128, v124 offset1:16
	ds_write2_b32 v178, v129, v125 offset0:32 offset1:48
	ds_write2_b32 v178, v130, v126 offset0:64 offset1:80
	ds_write2_b32 v178, v131, v127 offset0:96 offset1:112
	s_waitcnt lgkmcnt(0)
	s_barrier
	ds_read2st64_b32 v[124:125], v169 offset1:8
	ds_read2st64_b32 v[126:127], v169 offset0:16 offset1:24
	ds_read2st64_b32 v[128:129], v169 offset0:32 offset1:40
	s_waitcnt lgkmcnt(2)
	v_add_f32_e32 v124, v160, v124
	v_add_f32_e32 v130, v124, v125
	ds_read2st64_b32 v[124:125], v169 offset0:48 offset1:56
	s_waitcnt lgkmcnt(2)
	v_add_f32_e32 v126, v130, v126
	v_add_f32_e32 v126, v126, v127
	s_waitcnt lgkmcnt(1)
	v_add_f32_e32 v126, v126, v128
	v_add_f32_e32 v126, v126, v129
	s_waitcnt lgkmcnt(0)
	v_add_f32_e32 v124, v126, v124
	v_add_f32_e32 v126, v124, v125
	v_add_f32_e32 v126, 0, v126
	v_sub_u32_e32 v194, 31, v158
	v_ashrrev_i32_e32 v204, 31, v126
	v_or_b32_e32 v204, 0x80000000, v204
	v_xor_b32_e32 v195, v126, v204
	v_mov_b32_e32 v196, v194
	v_mov_b32_e32 v197, v195
	s_nop 1
	v_mov_b32_dpp v198, v196 row_ror:8 row_mask:0xf bank_mask:0xf
	v_mov_b32_dpp v199, v197 row_ror:8 row_mask:0xf bank_mask:0xf
	v_cmp_gt_u64_e32 vcc, v[198:199], v[196:197]
	s_nop 1
	v_cndmask_b32_e32 v196, v196, v198, vcc
	v_cndmask_b32_e32 v197, v197, v199, vcc
	s_nop 1
	v_mov_b32_dpp v198, v196 row_ror:4 row_mask:0xf bank_mask:0xf
	v_mov_b32_dpp v199, v197 row_ror:4 row_mask:0xf bank_mask:0xf
	v_cmp_gt_u64_e32 vcc, v[198:199], v[196:197]
	s_nop 1
	v_cndmask_b32_e32 v196, v196, v198, vcc
	v_cndmask_b32_e32 v197, v197, v199, vcc
	s_nop 1
	v_mov_b32_dpp v198, v196 row_ror:2 row_mask:0xf bank_mask:0xf
	v_mov_b32_dpp v199, v197 row_ror:2 row_mask:0xf bank_mask:0xf
	v_cmp_gt_u64_e32 vcc, v[198:199], v[196:197]
	s_nop 1
	v_cndmask_b32_e32 v196, v196, v198, vcc
	v_cndmask_b32_e32 v197, v197, v199, vcc
	s_nop 1
	v_mov_b32_dpp v198, v196 row_ror:1 row_mask:0xf bank_mask:0xf
	v_mov_b32_dpp v199, v197 row_ror:1 row_mask:0xf bank_mask:0xf
	v_cmp_gt_u64_e32 vcc, v[198:199], v[196:197]
	s_nop 1
	v_cndmask_b32_e32 v196, v196, v198, vcc
	v_cndmask_b32_e32 v197, v197, v199, vcc
	s_nop 1
	v_mov_b32_e32 v200, v196
	v_mov_b32_e32 v201, v197
	v_mov_b32_e32 v202, v196
	v_mov_b32_e32 v203, v197
	s_nop 1
	v_permlane16_swap_b32_e32 v200, v202
	v_permlane16_swap_b32_e32 v201, v203
	s_nop 1
	v_cmp_gt_u64_e32 vcc, v[202:203], v[200:201]
	s_nop 1
	v_cndmask_b32_e32 v196, v200, v202, vcc
	v_cndmask_b32_e32 v197, v201, v203, vcc
	v_ashrrev_i32_e32 v204, 31, v197
	v_xor_b32_e32 v204, -1, v204
	v_or_b32_e32 v204, 0x80000000, v204
	v_xor_b32_e32 v125, v197, v204
	v_sub_u32_e32 v124, 31, v196
	v_cmp_eq_u32_e32 vcc, v194, v196
	v_mov_b32_e32 v204, 0x7fffff
	s_nop 0
	v_cndmask_b32_e32 v195, v195, v204, vcc
	v_mov_b32_e32 v196, v194
	v_mov_b32_e32 v197, v195
	s_nop 1
	v_mov_b32_dpp v198, v196 row_ror:8 row_mask:0xf bank_mask:0xf
	v_mov_b32_dpp v199, v197 row_ror:8 row_mask:0xf bank_mask:0xf
	v_cmp_gt_u64_e32 vcc, v[198:199], v[196:197]
	s_nop 1
	v_cndmask_b32_e32 v196, v196, v198, vcc
	v_cndmask_b32_e32 v197, v197, v199, vcc
	s_nop 1
	v_mov_b32_dpp v198, v196 row_ror:4 row_mask:0xf bank_mask:0xf
	v_mov_b32_dpp v199, v197 row_ror:4 row_mask:0xf bank_mask:0xf
	v_cmp_gt_u64_e32 vcc, v[198:199], v[196:197]
	s_nop 1
	v_cndmask_b32_e32 v196, v196, v198, vcc
	v_cndmask_b32_e32 v197, v197, v199, vcc
	s_nop 1
	v_mov_b32_dpp v198, v196 row_ror:2 row_mask:0xf bank_mask:0xf
	v_mov_b32_dpp v199, v197 row_ror:2 row_mask:0xf bank_mask:0xf
	v_cmp_gt_u64_e32 vcc, v[198:199], v[196:197]
	s_nop 1
	v_cndmask_b32_e32 v196, v196, v198, vcc
	v_cndmask_b32_e32 v197, v197, v199, vcc
	s_nop 1
	v_mov_b32_dpp v198, v196 row_ror:1 row_mask:0xf bank_mask:0xf
	v_mov_b32_dpp v199, v197 row_ror:1 row_mask:0xf bank_mask:0xf
	v_cmp_gt_u64_e32 vcc, v[198:199], v[196:197]
	s_nop 1
	v_cndmask_b32_e32 v196, v196, v198, vcc
	v_cndmask_b32_e32 v197, v197, v199, vcc
	s_nop 1
	v_mov_b32_e32 v200, v196
	v_mov_b32_e32 v201, v197
	v_mov_b32_e32 v202, v196
	v_mov_b32_e32 v203, v197
	s_nop 1
	v_permlane16_swap_b32_e32 v200, v202
	v_permlane16_swap_b32_e32 v201, v203
	s_nop 1
	v_cmp_gt_u64_e32 vcc, v[202:203], v[200:201]
	s_nop 1
	v_cndmask_b32_e32 v196, v200, v202, vcc
	v_cndmask_b32_e32 v197, v201, v203, vcc
	v_ashrrev_i32_e32 v204, 31, v197
	v_xor_b32_e32 v204, -1, v204
	v_or_b32_e32 v204, 0x80000000, v204
	v_xor_b32_e32 v127, v197, v204
	v_sub_u32_e32 v126, 31, v196
	v_cmp_eq_u32_e32 vcc, v194, v196
	v_mov_b32_e32 v204, 0x7fffff
	s_nop 0
	v_cndmask_b32_e32 v195, v195, v204, vcc
	v_mov_b32_e32 v196, v194
	v_mov_b32_e32 v197, v195
	s_nop 1
	v_mov_b32_dpp v198, v196 row_ror:8 row_mask:0xf bank_mask:0xf
	v_mov_b32_dpp v199, v197 row_ror:8 row_mask:0xf bank_mask:0xf
	v_cmp_gt_u64_e32 vcc, v[198:199], v[196:197]
	s_nop 1
	v_cndmask_b32_e32 v196, v196, v198, vcc
	v_cndmask_b32_e32 v197, v197, v199, vcc
	s_nop 1
	v_mov_b32_dpp v198, v196 row_ror:4 row_mask:0xf bank_mask:0xf
	v_mov_b32_dpp v199, v197 row_ror:4 row_mask:0xf bank_mask:0xf
	v_cmp_gt_u64_e32 vcc, v[198:199], v[196:197]
	s_nop 1
	v_cndmask_b32_e32 v196, v196, v198, vcc
	v_cndmask_b32_e32 v197, v197, v199, vcc
	s_nop 1
	v_mov_b32_dpp v198, v196 row_ror:2 row_mask:0xf bank_mask:0xf
	v_mov_b32_dpp v199, v197 row_ror:2 row_mask:0xf bank_mask:0xf
	v_cmp_gt_u64_e32 vcc, v[198:199], v[196:197]
	s_nop 1
	v_cndmask_b32_e32 v196, v196, v198, vcc
	v_cndmask_b32_e32 v197, v197, v199, vcc
	s_nop 1
	v_mov_b32_dpp v198, v196 row_ror:1 row_mask:0xf bank_mask:0xf
	v_mov_b32_dpp v199, v197 row_ror:1 row_mask:0xf bank_mask:0xf
	v_cmp_gt_u64_e32 vcc, v[198:199], v[196:197]
	s_nop 1
	v_cndmask_b32_e32 v196, v196, v198, vcc
	v_cndmask_b32_e32 v197, v197, v199, vcc
	s_nop 1
	v_mov_b32_e32 v200, v196
	v_mov_b32_e32 v201, v197
	v_mov_b32_e32 v202, v196
	v_mov_b32_e32 v203, v197
	s_nop 1
	v_permlane16_swap_b32_e32 v200, v202
	v_permlane16_swap_b32_e32 v201, v203
	s_nop 1
	v_cmp_gt_u64_e32 vcc, v[202:203], v[200:201]
	s_nop 1
	v_cndmask_b32_e32 v196, v200, v202, vcc
	v_cndmask_b32_e32 v197, v201, v203, vcc
	v_ashrrev_i32_e32 v204, 31, v197
	v_xor_b32_e32 v204, -1, v204
	v_or_b32_e32 v204, 0x80000000, v204
	v_xor_b32_e32 v129, v197, v204
	v_sub_u32_e32 v128, 31, v196
	v_cmp_eq_u32_e32 vcc, v194, v196
	v_mov_b32_e32 v204, 0x7fffff
	s_nop 0
	v_cndmask_b32_e32 v195, v195, v204, vcc
	v_mov_b32_e32 v196, v194
	v_mov_b32_e32 v197, v195
	s_nop 1
	v_mov_b32_dpp v198, v196 row_ror:8 row_mask:0xf bank_mask:0xf
	v_mov_b32_dpp v199, v197 row_ror:8 row_mask:0xf bank_mask:0xf
	v_cmp_gt_u64_e32 vcc, v[198:199], v[196:197]
	s_nop 1
	v_cndmask_b32_e32 v196, v196, v198, vcc
	v_cndmask_b32_e32 v197, v197, v199, vcc
	s_nop 1
	v_mov_b32_dpp v198, v196 row_ror:4 row_mask:0xf bank_mask:0xf
	v_mov_b32_dpp v199, v197 row_ror:4 row_mask:0xf bank_mask:0xf
	v_cmp_gt_u64_e32 vcc, v[198:199], v[196:197]
	s_nop 1
	v_cndmask_b32_e32 v196, v196, v198, vcc
	v_cndmask_b32_e32 v197, v197, v199, vcc
	s_nop 1
	v_mov_b32_dpp v198, v196 row_ror:2 row_mask:0xf bank_mask:0xf
	v_mov_b32_dpp v199, v197 row_ror:2 row_mask:0xf bank_mask:0xf
	v_cmp_gt_u64_e32 vcc, v[198:199], v[196:197]
	s_nop 1
	v_cndmask_b32_e32 v196, v196, v198, vcc
	v_cndmask_b32_e32 v197, v197, v199, vcc
	s_nop 1
	v_mov_b32_dpp v198, v196 row_ror:1 row_mask:0xf bank_mask:0xf
	v_mov_b32_dpp v199, v197 row_ror:1 row_mask:0xf bank_mask:0xf
	v_cmp_gt_u64_e32 vcc, v[198:199], v[196:197]
	s_nop 1
	v_cndmask_b32_e32 v196, v196, v198, vcc
	v_cndmask_b32_e32 v197, v197, v199, vcc
	s_nop 1
	v_mov_b32_e32 v200, v196
	v_mov_b32_e32 v201, v197
	v_mov_b32_e32 v202, v196
	v_mov_b32_e32 v203, v197
	s_nop 1
	v_permlane16_swap_b32_e32 v200, v202
	v_permlane16_swap_b32_e32 v201, v203
	s_nop 1
	v_cmp_gt_u64_e32 vcc, v[202:203], v[200:201]
	s_nop 1
	v_cndmask_b32_e32 v196, v200, v202, vcc
	v_cndmask_b32_e32 v197, v201, v203, vcc
	v_ashrrev_i32_e32 v204, 31, v197
	v_xor_b32_e32 v204, -1, v204
	v_or_b32_e32 v204, 0x80000000, v204
	v_xor_b32_e32 v130, v197, v204
	v_sub_u32_e32 v131, 31, v196
	s_and_saveexec_b64 s[16:17], s[8:9]
	s_cbranch_execz .LBB0_870
